# phase D gate matmul: the twenty weight fragments of a trip requested together into twenty quads, consumed k-slice by k-slice with counted waits
# speedup vs baseline: 1.1990x; 1.0016x over previous
.LBB0_635:
	v_lshl_or_b32 v20, s41, 6, v76
	v_mad_i64_i32 v[54:55], s[50:51], v20, s22, v[34:35]
	v_or_b32_e32 v24, 16, v20
	v_or_b32_e32 v25, 32, v20
	v_or_b32_e32 v26, 48, v20
	v_mad_i64_i32 v[58:59], s[50:51], v24, s22, v[34:35]
	v_mad_i64_i32 v[60:61], s[50:51], v25, s22, v[34:35]
	v_mad_i64_i32 v[62:63], s[50:51], v26, s22, v[34:35]
	global_load_dwordx4 v[110:113], v[54:55], off
	global_load_dwordx4 v[130:133], v[58:59], off
	global_load_dwordx4 v[150:153], v[60:61], off
	global_load_dwordx4 v[216:219], v[62:63], off
	global_load_dwordx4 v[114:117], v[54:55], off offset:64
	global_load_dwordx4 v[134:137], v[58:59], off offset:64
	global_load_dwordx4 v[154:157], v[60:61], off offset:64
	global_load_dwordx4 v[220:223], v[62:63], off offset:64
	global_load_dwordx4 v[118:121], v[54:55], off offset:128
	global_load_dwordx4 v[138:141], v[58:59], off offset:128
	global_load_dwordx4 v[158:161], v[60:61], off offset:128
	global_load_dwordx4 v[224:227], v[62:63], off offset:128
	global_load_dwordx4 v[122:125], v[54:55], off offset:192
	global_load_dwordx4 v[142:145], v[58:59], off offset:192
	global_load_dwordx4 v[162:165], v[60:61], off offset:192
	global_load_dwordx4 v[228:231], v[62:63], off offset:192
	global_load_dwordx4 v[126:129], v[54:55], off offset:256
	global_load_dwordx4 v[146:149], v[58:59], off offset:256
	global_load_dwordx4 v[166:169], v[60:61], off offset:256
	global_load_dwordx4 v[232:235], v[62:63], off offset:256
	v_cndmask_b32_e64 v36, 0, 1, s[6:7]
	v_cmp_ne_u32_e32 vcc, 1, v36
	s_mov_b64 s[6:7], 0
	s_and_b64 vcc, exec, vcc
	s_waitcnt vmcnt(16) lgkmcnt(4)
	v_mfma_f32_16x16x32_bf16 v[20:23], v[110:113], v[0:3], 0
	v_mfma_f32_16x16x32_bf16 v[24:27], v[130:133], v[0:3], 0
	v_mfma_f32_16x16x32_bf16 v[38:41], v[150:153], v[0:3], 0
	v_mfma_f32_16x16x32_bf16 v[42:45], v[216:219], v[0:3], 0
	s_waitcnt vmcnt(12) lgkmcnt(3)
	v_mfma_f32_16x16x32_bf16 v[20:23], v[114:117], v[4:7], v[20:23]
	v_mfma_f32_16x16x32_bf16 v[24:27], v[134:137], v[4:7], v[24:27]
	v_mfma_f32_16x16x32_bf16 v[38:41], v[154:157], v[4:7], v[38:41]
	v_mfma_f32_16x16x32_bf16 v[42:45], v[220:223], v[4:7], v[42:45]
	s_waitcnt vmcnt(8) lgkmcnt(2)
	v_mfma_f32_16x16x32_bf16 v[20:23], v[118:121], v[8:11], v[20:23]
	v_mfma_f32_16x16x32_bf16 v[24:27], v[138:141], v[8:11], v[24:27]
	v_mfma_f32_16x16x32_bf16 v[38:41], v[158:161], v[8:11], v[38:41]
	v_mfma_f32_16x16x32_bf16 v[42:45], v[224:227], v[8:11], v[42:45]
	s_waitcnt vmcnt(4) lgkmcnt(1)
	v_mfma_f32_16x16x32_bf16 v[20:23], v[122:125], v[12:15], v[20:23]
	v_mfma_f32_16x16x32_bf16 v[24:27], v[142:145], v[12:15], v[24:27]
	v_mfma_f32_16x16x32_bf16 v[38:41], v[162:165], v[12:15], v[38:41]
	v_mfma_f32_16x16x32_bf16 v[42:45], v[228:231], v[12:15], v[42:45]
	s_waitcnt vmcnt(0) lgkmcnt(0)
	v_mfma_f32_16x16x32_bf16 v[20:23], v[126:129], v[16:19], v[20:23]
	v_mfma_f32_16x16x32_bf16 v[24:27], v[146:149], v[16:19], v[24:27]
	v_mfma_f32_16x16x32_bf16 v[38:41], v[166:169], v[16:19], v[38:41]
	v_mfma_f32_16x16x32_bf16 v[42:45], v[232:235], v[16:19], v[42:45]
	v_lshl_add_u32 v50, s41, 7, v78
	s_mov_b32 s41, 1
	v_add_u32_e32 v36, 0x2800, v50
	s_nop 7
	s_nop 3
	v_cvt_pk_bf16_f32 v20, v20, v21
	v_cvt_pk_bf16_f32 v21, v22, v23
	v_cvt_pk_bf16_f32 v22, v24, v25
	v_cvt_pk_bf16_f32 v23, v26, v27
	v_cvt_pk_bf16_f32 v24, v38, v39
	v_cvt_pk_bf16_f32 v25, v40, v41
	v_cvt_pk_bf16_f32 v26, v42, v43
	v_cvt_pk_bf16_f32 v27, v44, v45
	ds_write2_b64 v36, v[20:21], v[22:23] offset0:64 offset1:68
	ds_write2_b64 v36, v[24:25], v[26:27] offset0:72 offset1:76
	s_cbranch_vccz .LBB0_635
	s_waitcnt lgkmcnt(0)
	s_barrier
